# v30
# speedup vs baseline: 1.0087x; 1.0064x over previous
.LBB0_6:
	v_lshl_add_u64 v[46:47], v[2:3], 0, s[0:1]
	v_lshl_add_u64 v[50:51], v[4:5], 0, s[0:1]
	global_load_dwordx4 v[10:13], v[46:47], off nt
	global_load_dwordx4 v[14:17], v[50:51], off
	global_load_dwordx4 v[18:21], v[46:47], off offset:16 nt
	global_load_dwordx4 v[22:25], v[46:47], off offset:128 nt
	global_load_dwordx4 v[26:29], v[46:47], off offset:144 nt
	global_load_dwordx4 v[30:33], v[46:47], off offset:256 nt
	global_load_dwordx4 v[34:37], v[46:47], off offset:272 nt
	s_add_u32 s0, s0, 0x200
	s_addc_u32 s1, s1, 0
	s_cmpk_eq_i32 s0, 0x1000
	s_waitcnt vmcnt(5)
	v_mfma_f32_16x16x4_f32 a[0:3], v10, v14, a[0:3]
	v_cvt_pkrtz_f16_f32 v10, v10, v11
	v_add_u32_e32 v10, 0x20002, v10
	v_and_b32_e32 v10, 0xfffcfffc, v10
	v_mfma_f32_16x16x4_f32 a[0:3], v11, v15, a[0:3]
	v_cvt_pkrtz_f16_f32 v11, v12, v13
	v_add_u32_e32 v11, 0x20002, v11
	v_and_b32_e32 v11, 0xfffcfffc, v11
	v_mfma_f32_16x16x4_f32 a[0:3], v12, v16, a[0:3]
	s_waitcnt vmcnt(4)
	v_cvt_pkrtz_f16_f32 v12, v18, v19
	v_add_u32_e32 v12, 0x20002, v12
	v_and_b32_e32 v12, 0xfffcfffc, v12
	v_mfma_f32_16x16x4_f32 a[0:3], v13, v17, a[0:3]
	global_load_dwordx4 v[14:17], v[50:51], off offset:16
	v_cvt_pkrtz_f16_f32 v13, v20, v21
	v_add_u32_e32 v13, 0x20002, v13
	v_and_b32_e32 v13, 0xfffcfffc, v13
	s_waitcnt vmcnt(0)
	v_mfma_f32_16x16x4_f32 a[0:3], v18, v14, a[0:3]
	v_cvt_pkrtz_f16_f32 v18, v22, v23
	v_add_u32_e32 v18, 0x20002, v18
	v_and_b32_e32 v18, 0xfffcfffc, v18
	v_mfma_f32_16x16x4_f32 a[0:3], v19, v15, a[0:3]
	v_cvt_pkrtz_f16_f32 v19, v24, v25
	v_add_u32_e32 v19, 0x20002, v19
	v_and_b32_e32 v19, 0xfffcfffc, v19
	v_mfma_f32_16x16x4_f32 a[0:3], v20, v16, a[0:3]
	v_cvt_pkrtz_f16_f32 v20, v26, v27
	v_add_u32_e32 v20, 0x20002, v20
	v_and_b32_e32 v20, 0xfffcfffc, v20
	v_mfma_f32_16x16x4_f32 a[0:3], v21, v17, a[0:3]
	global_load_dwordx4 v[14:17], v[50:51], off offset:128
	v_cvt_pkrtz_f16_f32 v21, v28, v29
	v_add_u32_e32 v21, 0x20002, v21
	v_and_b32_e32 v21, 0xfffcfffc, v21
	s_waitcnt vmcnt(0)
	v_mfma_f32_16x16x4_f32 a[0:3], v22, v14, a[0:3]
	v_cvt_pkrtz_f16_f32 v22, v30, v31
	v_add_u32_e32 v22, 0x20002, v22
	v_and_b32_e32 v22, 0xfffcfffc, v22
	v_mfma_f32_16x16x4_f32 a[0:3], v23, v15, a[0:3]
	v_cvt_pkrtz_f16_f32 v23, v32, v33
	v_mfma_f32_16x16x4_f32 a[0:3], v24, v16, a[0:3]
	v_cvt_pkrtz_f16_f32 v24, v34, v35
	v_add_u32_e32 v24, 0x20002, v24
	v_and_b32_e32 v24, 0xfffcfffc, v24
	v_mfma_f32_16x16x4_f32 a[0:3], v25, v17, a[0:3]
	global_load_dwordx4 v[14:17], v[50:51], off offset:144
	v_cvt_pkrtz_f16_f32 v25, v36, v37
	v_add_u32_e32 v25, 0x20002, v25
	v_and_b32_e32 v25, 0xfffcfffc, v25
	s_waitcnt vmcnt(0)
	v_mfma_f32_16x16x4_f32 a[0:3], v26, v14, a[0:3]
	v_mfma_f32_16x16x4_f32 a[0:3], v27, v15, a[0:3]
	v_mfma_f32_16x16x4_f32 a[0:3], v28, v16, a[0:3]
	v_mfma_f32_16x16x4_f32 a[0:3], v29, v17, a[0:3]
	global_load_dwordx4 v[14:17], v[50:51], off offset:256
	s_waitcnt vmcnt(0)
	v_mfma_f32_16x16x4_f32 a[0:3], v30, v14, a[0:3]
	v_mfma_f32_16x16x4_f32 a[0:3], v31, v15, a[0:3]
	v_mfma_f32_16x16x4_f32 a[0:3], v32, v16, a[0:3]
	v_mfma_f32_16x16x4_f32 a[0:3], v33, v17, a[0:3]
	global_load_dwordx4 v[14:17], v[50:51], off offset:272
	global_load_dwordx4 v[38:41], v[46:47], off offset:384 nt
	global_load_dwordx4 v[42:45], v[46:47], off offset:400 nt
	s_waitcnt vmcnt(1)
	v_cvt_pkrtz_f16_f32 v26, v38, v39
	global_load_dwordx4 v[46:49], v[50:51], off offset:384
	v_mfma_f32_16x16x4_f32 a[0:3], v34, v14, a[0:3]
	v_cvt_pkrtz_f16_f32 v27, v40, v41
	s_waitcnt vmcnt(1)
	v_cvt_pkrtz_f16_f32 v28, v42, v43
	v_cvt_pkrtz_f16_f32 v29, v44, v45
	v_add_u32_e32 v26, 0x20002, v26
	v_add_u32_e32 v27, 0x20002, v27
	v_add_u32_e32 v28, 0x20002, v28
	v_add_u32_e32 v29, 0x20002, v29
	v_mfma_f32_16x16x4_f32 a[0:3], v35, v15, a[0:3]
	v_mfma_f32_16x16x4_f32 a[0:3], v36, v16, a[0:3]
	v_mfma_f32_16x16x4_f32 a[0:3], v37, v17, a[0:3]
	global_load_dwordx4 v[14:17], v[50:51], off offset:400
	s_waitcnt vmcnt(1)
	v_mfma_f32_16x16x4_f32 a[0:3], v38, v46, a[0:3]
	v_mfma_f32_16x16x4_f32 a[0:3], v39, v47, a[0:3]
	v_mfma_f32_16x16x4_f32 a[0:3], v40, v48, a[0:3]
	v_mfma_f32_16x16x4_f32 a[0:3], v41, v49, a[0:3]
	s_waitcnt vmcnt(0)
	v_mfma_f32_16x16x4_f32 a[0:3], v42, v14, a[0:3]
	v_add_u32_e32 v14, 0x20002, v23
	v_and_b32_e32 v23, 0xfffcfffc, v14
	v_and_b32_e32 v14, 0xfffcfffc, v26
	v_mfma_f32_16x16x4_f32 a[0:3], v43, v15, a[0:3]
	v_and_b32_e32 v15, 0xfffcfffc, v27
	v_mfma_f32_16x16x4_f32 a[0:3], v44, v16, a[0:3]
	v_and_b32_e32 v16, 0xfffcfffc, v28
	v_mfma_f32_16x16x4_f32 a[0:3], v45, v17, a[0:3]
	v_and_b32_e32 v17, 0xfffcfffc, v29
	global_store_dwordx4 v[6:7], v[10:13], off offset:-128
	global_store_dwordx4 v[6:7], v[18:21], off offset:-64
	global_store_dwordx4 v[6:7], v[22:25], off
	global_store_dwordx4 v[6:7], v[14:17], off offset:64
	v_lshl_add_u64 v[6:7], v[6:7], 0, s[2:3]
	s_cbranch_scc0 .LBB0_6
	v_mul_u32_u24_e32 v2, 0x440, v8
	v_mul_u32_u24_e32 v3, 0x110, v9
	v_lshlrev_b32_e32 v1, 2, v1
	v_add3_u32 v1, v2, v3, v1
	v_cmp_gt_u32_e32 vcc, 16, v0
	ds_write_b32 v1, a0
	ds_write_b32 v1, a1 offset:68
	ds_write_b32 v1, a2 offset:136
	ds_write_b32 v1, a3 offset:204
	s_waitcnt lgkmcnt(0)
	s_barrier
	s_and_saveexec_b64 s[0:1], vcc
	s_cbranch_execz .LBB0_13
	s_movk_i32 s0, 0x44
	v_mov_b32_e32 v2, 0x440
	v_mov_b32_e32 v3, 0x880
	v_mov_b32_e32 v4, 0xcc0
	v_mul_u32_u24_e32 v1, 0x44, v0
	v_mad_u32_u24 v2, v0, s0, v2
	v_mad_u32_u24 v3, v0, s0, v3
	v_mad_u32_u24 v4, v0, s0, v4
	ds_read2_b32 v[10:11], v1 offset1:1
	ds_read2_b32 v[12:13], v2 offset1:1
	ds_read2_b32 v[2:3], v3 offset1:1
	ds_read2_b32 v[4:5], v4 offset1:1
	ds_read2_b32 v[16:17], v1 offset0:2 offset1:3
	ds_read2_b32 v[18:19], v1 offset0:4 offset1:5
	ds_read2_b32 v[20:21], v1 offset0:6 offset1:7
	s_waitcnt lgkmcnt(4)
	v_mov_b32_e32 v7, v2
	s_waitcnt lgkmcnt(3)
	v_mov_b32_e32 v9, v4
	v_mov_b32_e32 v2, v11
	v_mov_b32_e32 v4, v13
	v_pk_add_f32 v[2:3], v[2:3], v[4:5]
	v_mov_b32_e32 v6, v10
	v_mov_b32_e32 v1, 0x448
	v_mov_b32_e32 v8, v12
	v_add_f32_e32 v14, v2, v3
	v_mov_b32_e32 v2, 0x888
	v_mad_u32_u24 v1, v0, s0, v1
	v_pk_add_f32 v[6:7], v[6:7], v[8:9]
	v_mad_u32_u24 v2, v0, s0, v2
	ds_read2_b32 v[22:23], v1 offset1:1
	ds_read2_b32 v[2:3], v2 offset1:1
	v_add_f32_e32 v1, v6, v7
	v_mov_b32_e32 v6, 0x450
	v_mov_b32_e32 v4, 0xcc8
	v_mad_u32_u24 v8, v0, s0, v6
	v_mov_b32_e32 v6, 0x890
	v_mad_u32_u24 v5, v0, s0, v4
	v_mad_u32_u24 v9, v0, s0, v6
	ds_read2_b32 v[6:7], v5 offset1:1
	ds_read2_b32 v[24:25], v8 offset1:1
	ds_read2_b32 v[8:9], v9 offset1:1
	s_waitcnt lgkmcnt(3)
	v_mov_b32_e32 v5, v2
	v_mov_b32_e32 v2, v17
	s_waitcnt lgkmcnt(2)
	v_mov_b32_e32 v11, v6
	v_mov_b32_e32 v6, v23
	v_pk_add_f32 v[2:3], v[2:3], v[6:7]
	v_mov_b32_e32 v4, v16
	v_add_f32_e32 v16, v2, v3
	v_mov_b32_e32 v2, 0xcd0
	v_mov_b32_e32 v10, v22
	v_mad_u32_u24 v2, v0, s0, v2
	v_pk_add_f32 v[4:5], v[4:5], v[10:11]
	ds_read2_b32 v[2:3], v2 offset1:1
	v_mov_b32_e32 v7, 0x458
	v_mov_b32_e32 v10, 0xcd8
	v_add_f32_e32 v15, v4, v5
	s_waitcnt lgkmcnt(1)
	v_mov_b32_e32 v5, v8
	v_mad_u32_u24 v7, v0, s0, v7
	v_mov_b32_e32 v8, 0x898
	v_mad_u32_u24 v12, v0, s0, v10
	v_mad_u32_u24 v8, v0, s0, v8
	ds_read2_b32 v[22:23], v7 offset1:1
	ds_read2_b32 v[10:11], v8 offset1:1
	ds_read2_b32 v[12:13], v12 offset1:1
	v_mov_b32_e32 v4, v18
	v_mov_b32_e32 v6, v24
	s_waitcnt lgkmcnt(3)
	v_mov_b32_e32 v7, v2
	v_mov_b32_e32 v8, v19
	v_mov_b32_e32 v2, v25
	v_pk_add_f32 v[4:5], v[4:5], v[6:7]
	v_pk_add_f32 v[2:3], v[8:9], v[2:3]
	v_add_f32_e32 v6, v4, v5
	v_add_f32_e32 v7, v2, v3
	v_mov_b32_e32 v2, v20
	s_waitcnt lgkmcnt(1)
	v_mov_b32_e32 v3, v10
	v_mov_b32_e32 v4, v22
	s_waitcnt lgkmcnt(0)
	v_mov_b32_e32 v5, v12
	v_pk_add_f32 v[2:3], v[2:3], v[4:5]
	v_mov_b32_e32 v10, v21
	v_mov_b32_e32 v12, v23
	v_add_f32_e32 v4, v2, v3
	v_pk_add_f32 v[2:3], v[10:11], v[12:13]
	s_mov_b32 s0, 0x3fb8aa3b
	v_add_f32_e32 v2, v2, v3
	v_max_f32_e32 v3, v1, v14
	v_max3_f32 v3, v3, v15, v16
	v_max3_f32 v3, v3, v6, v7
	v_max3_f32 v3, v3, v4, v2
	v_sub_f32_e32 v1, v1, v3
	v_mul_f32_e32 v5, 0x3fb8aa3b, v1
	v_fma_f32 v8, v1, s0, -v5
	v_rndne_f32_e32 v9, v5
	v_fmac_f32_e32 v8, 0x32a5705f, v1
	v_sub_f32_e32 v5, v5, v9
	v_add_f32_e32 v5, v5, v8
	v_exp_f32_e32 v5, v5
	v_cvt_i32_f32_e32 v8, v9
	s_mov_b32 s1, 0xc2ce8ed0
	v_cmp_ngt_f32_e32 vcc, s1, v1
	s_mov_b32 s2, 0x42b17218
	v_ldexp_f32 v5, v5, v8
	v_sub_f32_e32 v8, v14, v3
	v_mul_f32_e32 v9, 0x3fb8aa3b, v8
	v_fma_f32 v10, v8, s0, -v9
	v_rndne_f32_e32 v11, v9
	v_fmac_f32_e32 v10, 0x32a5705f, v8
	v_sub_f32_e32 v9, v9, v11
	v_add_f32_e32 v9, v9, v10
	v_exp_f32_e32 v9, v9
	v_cvt_i32_f32_e32 v10, v11
	v_cndmask_b32_e32 v5, 0, v5, vcc
	v_mov_b32_e32 v11, 0x7f800000
	v_cmp_nlt_f32_e32 vcc, s2, v1
	v_sub_f32_e32 v6, v6, v3
	v_sub_f32_e32 v7, v7, v3
	v_cndmask_b32_e32 v1, v11, v5, vcc
	v_ldexp_f32 v5, v9, v10
	v_sub_f32_e32 v9, v15, v3
	v_mul_f32_e32 v10, 0x3fb8aa3b, v9
	v_fma_f32 v12, v9, s0, -v10
	v_rndne_f32_e32 v13, v10
	v_fmac_f32_e32 v12, 0x32a5705f, v9
	v_sub_f32_e32 v10, v10, v13
	v_add_f32_e32 v10, v10, v12
	v_exp_f32_e32 v10, v10
	v_cvt_i32_f32_e32 v12, v13
	v_cmp_ngt_f32_e32 vcc, s1, v8
	v_sub_f32_e32 v4, v4, v3
	v_sub_f32_e32 v2, v2, v3
	v_ldexp_f32 v10, v10, v12
	v_sub_f32_e32 v12, v16, v3
	v_mul_f32_e32 v13, 0x3fb8aa3b, v12
	v_fma_f32 v14, v12, s0, -v13
	v_rndne_f32_e32 v15, v13
	v_fmac_f32_e32 v14, 0x32a5705f, v12
	v_sub_f32_e32 v13, v13, v15
	v_add_f32_e32 v13, v13, v14
	v_exp_f32_e32 v13, v13
	v_cvt_i32_f32_e32 v14, v15
	v_cndmask_b32_e32 v5, 0, v5, vcc
	v_cmp_nlt_f32_e32 vcc, s2, v8
	v_mul_f32_e32 v3, 0x3fb8aa3b, v2
	s_nop 0
	v_cndmask_b32_e32 v5, v11, v5, vcc
	v_cmp_ngt_f32_e32 vcc, s1, v9
	v_add_f32_e32 v8, v1, v5
	s_nop 0
	v_cndmask_b32_e32 v10, 0, v10, vcc
	v_cmp_nlt_f32_e32 vcc, s2, v9
	s_nop 1
	v_cndmask_b32_e32 v9, v11, v10, vcc
	v_ldexp_f32 v10, v13, v14
	v_mul_f32_e32 v13, 0x3fb8aa3b, v6
	v_fma_f32 v14, v6, s0, -v13
	v_rndne_f32_e32 v15, v13
	v_fmac_f32_e32 v14, 0x32a5705f, v6
	v_sub_f32_e32 v13, v13, v15
	v_add_f32_e32 v13, v13, v14
	v_exp_f32_e32 v13, v13
	v_cvt_i32_f32_e32 v14, v15
	v_cmp_ngt_f32_e32 vcc, s1, v12
	v_add_f32_e32 v8, v9, v8
	s_nop 0
	v_cndmask_b32_e32 v10, 0, v10, vcc
	v_cmp_nlt_f32_e32 vcc, s2, v12
	v_ldexp_f32 v12, v13, v14
	v_mul_f32_e32 v13, 0x3fb8aa3b, v7
	v_fma_f32 v14, v7, s0, -v13
	v_rndne_f32_e32 v15, v13
	v_fmac_f32_e32 v14, 0x32a5705f, v7
	v_sub_f32_e32 v13, v13, v15
	v_add_f32_e32 v13, v13, v14
	v_exp_f32_e32 v13, v13
	v_cvt_i32_f32_e32 v14, v15
	v_cndmask_b32_e32 v10, v11, v10, vcc
	v_cmp_ngt_f32_e32 vcc, s1, v6
	v_add_f32_e32 v8, v10, v8
	s_nop 0
	v_cndmask_b32_e32 v12, 0, v12, vcc
	v_cmp_nlt_f32_e32 vcc, s2, v6
	s_nop 1
	v_cndmask_b32_e32 v6, v11, v12, vcc
	v_ldexp_f32 v12, v13, v14
	v_mul_f32_e32 v13, 0x3fb8aa3b, v4
	v_fma_f32 v14, v4, s0, -v13
	v_rndne_f32_e32 v15, v13
	v_fmac_f32_e32 v14, 0x32a5705f, v4
	v_sub_f32_e32 v13, v13, v15
	v_add_f32_e32 v13, v13, v14
	v_exp_f32_e32 v13, v13
	v_cvt_i32_f32_e32 v14, v15
	v_cmp_ngt_f32_e32 vcc, s1, v7
	v_add_f32_e32 v8, v6, v8
	s_nop 0
	v_cndmask_b32_e32 v12, 0, v12, vcc
	v_cmp_nlt_f32_e32 vcc, s2, v7
	s_nop 1
	v_cndmask_b32_e32 v7, v11, v12, vcc
	v_ldexp_f32 v12, v13, v14
	v_fma_f32 v13, v2, s0, -v3
	v_rndne_f32_e32 v14, v3
	v_fmac_f32_e32 v13, 0x32a5705f, v2
	v_sub_f32_e32 v3, v3, v14
	v_add_f32_e32 v3, v3, v13
	v_exp_f32_e32 v3, v3
	v_cvt_i32_f32_e32 v13, v14
	v_cmp_ngt_f32_e32 vcc, s1, v4
	v_add_f32_e32 v8, v7, v8
	v_ldexp_f32 v3, v3, v13
	v_cndmask_b32_e32 v12, 0, v12, vcc
	v_cmp_nlt_f32_e32 vcc, s2, v4
	s_nop 1
	v_cndmask_b32_e32 v4, v11, v12, vcc
	v_cmp_ngt_f32_e32 vcc, s1, v2
	v_add_f32_e32 v8, v4, v8
	s_nop 0
	v_cndmask_b32_e32 v3, 0, v3, vcc
	v_cmp_nlt_f32_e32 vcc, s2, v2
	s_nop 1
	v_cndmask_b32_e32 v2, v11, v3, vcc
	v_add_f32_e32 v3, v2, v8
	v_div_scale_f32 v8, s[0:1], v3, v3, v1
	v_rcp_f32_e32 v11, v8
	s_nop 0
	v_fma_f32 v12, -v8, v11, 1.0
	v_fmac_f32_e32 v11, v12, v11
	v_div_scale_f32 v12, vcc, v1, v3, v1
	v_mul_f32_e32 v13, v12, v11
	v_fma_f32 v14, -v8, v13, v12
	v_fmac_f32_e32 v13, v14, v11
	v_fma_f32 v8, -v8, v13, v12
	v_div_scale_f32 v12, s[0:1], v3, v3, v5
	v_rcp_f32_e32 v14, v12
	v_div_fmas_f32 v8, v8, v11, v13
	v_div_fixup_f32 v8, v8, v3, v1
	v_cmp_lt_f32_e64 s[6:7], -1.0, v8
	v_fma_f32 v1, -v12, v14, 1.0
	v_fmac_f32_e32 v14, v1, v14
	v_div_scale_f32 v1, vcc, v5, v3, v5
	v_mul_f32_e32 v11, v1, v14
	v_fma_f32 v13, -v12, v11, v1
	v_fmac_f32_e32 v11, v13, v14
	v_fma_f32 v1, -v12, v11, v1
	v_div_scale_f32 v12, s[0:1], v3, v3, v9
	v_rcp_f32_e32 v13, v12
	v_div_fmas_f32 v1, v1, v14, v11
	v_div_fixup_f32 v5, v1, v3, v5
	v_fma_f32 v1, -v12, v13, 1.0
	v_fmac_f32_e32 v13, v1, v13
	v_div_scale_f32 v1, vcc, v9, v3, v9
	v_mul_f32_e32 v11, v1, v13
	v_fma_f32 v14, -v12, v11, v1
	v_fmac_f32_e32 v11, v14, v13
	v_fma_f32 v1, -v12, v11, v1
	v_div_scale_f32 v12, s[0:1], v3, v3, v10
	v_rcp_f32_e32 v14, v12
	v_div_fmas_f32 v1, v1, v13, v11
	v_div_fixup_f32 v9, v1, v3, v9
	v_fma_f32 v1, -v12, v14, 1.0
	v_fmac_f32_e32 v14, v1, v14
	v_div_scale_f32 v1, vcc, v10, v3, v10
	v_mul_f32_e32 v11, v1, v14
	v_fma_f32 v13, -v12, v11, v1
	v_fmac_f32_e32 v11, v13, v14
	v_fma_f32 v1, -v12, v11, v1
	v_div_scale_f32 v12, s[0:1], v3, v3, v6
	v_rcp_f32_e32 v13, v12
	v_div_fmas_f32 v1, v1, v14, v11
	v_div_fixup_f32 v10, v1, v3, v10
	v_fma_f32 v1, -v12, v13, 1.0
	v_fmac_f32_e32 v13, v1, v13
	v_div_scale_f32 v1, vcc, v6, v3, v6
	v_mul_f32_e32 v11, v1, v13
	v_fma_f32 v14, -v12, v11, v1
	v_fmac_f32_e32 v11, v14, v13
	v_fma_f32 v1, -v12, v11, v1
	v_div_scale_f32 v12, s[0:1], v3, v3, v7
	v_rcp_f32_e32 v14, v12
	v_div_fmas_f32 v1, v1, v13, v11
	v_div_fixup_f32 v6, v1, v3, v6
	v_fma_f32 v1, -v12, v14, 1.0
	v_fmac_f32_e32 v14, v1, v14
	v_div_scale_f32 v1, vcc, v7, v3, v7
	v_mul_f32_e32 v11, v1, v14
	v_fma_f32 v13, -v12, v11, v1
	v_fmac_f32_e32 v11, v13, v14
	v_fma_f32 v1, -v12, v11, v1
	v_div_scale_f32 v12, s[0:1], v3, v3, v4
	v_rcp_f32_e32 v13, v12
	v_div_fmas_f32 v1, v1, v14, v11
	v_div_fixup_f32 v7, v1, v3, v7
	v_fma_f32 v1, -v12, v13, 1.0
	v_fmac_f32_e32 v13, v1, v13
	v_div_scale_f32 v1, vcc, v4, v3, v4
	v_mul_f32_e32 v11, v1, v13
	v_fma_f32 v14, -v12, v11, v1
	v_fmac_f32_e32 v11, v14, v13
	v_fma_f32 v1, -v12, v11, v1
	v_div_scale_f32 v12, s[0:1], v3, v3, v2
	v_rcp_f32_e32 v14, v12
	v_div_fmas_f32 v1, v1, v13, v11
	v_div_fixup_f32 v4, v1, v3, v4
	v_fma_f32 v1, -v12, v14, 1.0
	v_fmac_f32_e32 v14, v1, v14
	v_div_scale_f32 v1, vcc, v2, v3, v2
	v_mul_f32_e32 v11, v1, v14
	v_fma_f32 v13, -v12, v11, v1
	v_fmac_f32_e32 v11, v13, v14
	v_fma_f32 v1, -v12, v11, v1
	v_div_fmas_f32 v1, v1, v14, v11
	v_cmp_gt_f32_e32 vcc, v5, v8
	v_div_fixup_f32 v1, v1, v3, v2
	s_nop 0
	v_cndmask_b32_e32 v3, v8, v5, vcc
	v_cndmask_b32_e64 v2, 0, 1, vcc
	v_cmp_gt_f32_e32 vcc, v9, v3
	s_nop 1
	v_cndmask_b32_e32 v3, v3, v9, vcc
	v_cndmask_b32_e64 v2, v2, 2, vcc
	v_cmp_gt_f32_e32 vcc, v10, v3
	s_nop 1
	v_cndmask_b32_e32 v3, v3, v10, vcc
	v_cndmask_b32_e64 v2, v2, 3, vcc
	v_cmp_gt_f32_e32 vcc, v6, v3
	s_nop 1
	v_cndmask_b32_e32 v3, v3, v6, vcc
	v_cndmask_b32_e64 v2, v2, 4, vcc
	v_cmp_gt_f32_e32 vcc, v7, v3
	s_nop 1
	v_cndmask_b32_e32 v3, v3, v7, vcc
	v_cndmask_b32_e64 v2, v2, 5, vcc
	v_cmp_ngt_f32_e32 vcc, v4, v3
	s_nop 1
	v_cndmask_b32_e32 v3, v4, v3, vcc
	v_cndmask_b32_e32 v2, 6, v2, vcc
	v_cmp_gt_f32_e64 s[2:3], v1, v3
	v_cmp_ngt_f32_e64 s[0:1], v1, v3
	s_nop 0
	v_cndmask_b32_e64 v2, v2, 7, s[2:3]
	v_cmp_ne_u32_e64 s[4:5], 0, v2
	s_and_b64 s[4:5], s[6:7], s[4:5]
	s_or_b64 s[2:3], vcc, s[2:3]
	v_cndmask_b32_e64 v8, -1.0, v8, s[4:5]
	v_cmp_ne_u32_e64 s[4:5], 1, v2
	v_cmp_gt_f32_e64 s[6:7], v5, v8
	s_and_b64 s[4:5], s[4:5], s[6:7]
	v_cndmask_b32_e64 v5, v8, v5, s[4:5]
	v_cmp_ne_u32_e64 s[4:5], 2, v2
	v_cmp_gt_f32_e64 s[6:7], v9, v5
	s_and_b64 s[4:5], s[4:5], s[6:7]
	v_cndmask_b32_e64 v5, v5, v9, s[4:5]
	v_cmp_ne_u32_e64 s[4:5], 3, v2
	v_cmp_gt_f32_e64 s[6:7], v10, v5
	s_and_b64 s[4:5], s[4:5], s[6:7]
	v_cndmask_b32_e64 v5, v5, v10, s[4:5]
	v_cmp_ne_u32_e64 s[4:5], 4, v2
	v_cmp_gt_f32_e64 s[6:7], v6, v5
	s_and_b64 s[4:5], s[4:5], s[6:7]
	v_cndmask_b32_e64 v5, v5, v6, s[4:5]
	v_cmp_ne_u32_e64 s[4:5], 5, v2
	v_cmp_gt_f32_e64 s[6:7], v7, v5
	s_and_b64 s[4:5], s[4:5], s[6:7]
	v_cndmask_b32_e64 v2, v5, v7, s[4:5]
	v_cmp_gt_f32_e32 vcc, v4, v2
	s_and_b64 vcc, s[2:3], vcc
	s_nop 0
	v_cndmask_b32_e32 v2, v2, v4, vcc
	s_and_saveexec_b64 s[2:3], s[0:1]
	s_cbranch_execz .LBB0_12
	v_cmp_gt_f32_e32 vcc, v1, v2
	s_and_saveexec_b64 s[0:1], vcc
	v_mov_b32_e32 v2, v1
	s_or_b64 exec, exec, s[0:1]
	v_mov_b32_e32 v1, v3
